# baseline (speedup 1.0000x reference)
_Z11center_prepPKfPcPfS2_:
	s_load_dwordx2 s[6:7], s[0:1], 0x0
	s_load_dwordx4 s[8:11], s[0:1], 0x8
	s_load_dwordx2 s[12:13], s[0:1], 0x18
	v_lshrrev_b32_e32 v1, 3, v0
	v_and_b32_e32 v2, 7, v0
	v_lshlrev_b32_e32 v3, 10, v1
	v_lshl_or_b32 v136, v2, 4, v3
	v_mul_u32_u24_e32 v3, 0x110, v1
	v_lshl_add_u32 v137, v2, 4, v3
	v_and_b32_e32 v4, 31, v0
	v_lshrrev_b32_e32 v5, 5, v0
	v_mul_u32_u24_e32 v3, 0x110, v4
	v_lshl_add_u32 v138, v5, 5, v3
	v_lshlrev_b32_e32 v139, 5, v0
	v_lshlrev_b32_e32 v140, 2, v1
	v_mov_b32_e32 v142, -2.0
	v_mov_b32_e32 v143, -2.0
	s_lshl_b32 s14, s2, 15
	s_waitcnt lgkmcnt(0)
	s_add_u32 s16, s6, s14
	s_addc_u32 s17, s7, 0
	global_load_dwordx4 v[8:11], v136, s[16:17] offset:0 nt
	global_load_dwordx4 v[12:15], v136, s[16:17] offset:128 nt
	global_load_dwordx4 v[16:19], v136, s[16:17] offset:256 nt
	global_load_dwordx4 v[20:23], v136, s[16:17] offset:384 nt
	global_load_dwordx4 v[24:27], v136, s[16:17] offset:512 nt
	global_load_dwordx4 v[28:31], v136, s[16:17] offset:640 nt
	global_load_dwordx4 v[32:35], v136, s[16:17] offset:768 nt
	global_load_dwordx4 v[36:39], v136, s[16:17] offset:896 nt
	s_add_u32 s18, s16, 0x2000
	s_addc_u32 s19, s17, 0
	global_load_dwordx4 v[40:43], v136, s[18:19] offset:0 nt
	global_load_dwordx4 v[44:47], v136, s[18:19] offset:128 nt
	global_load_dwordx4 v[48:51], v136, s[18:19] offset:256 nt
	global_load_dwordx4 v[52:55], v136, s[18:19] offset:384 nt
	global_load_dwordx4 v[56:59], v136, s[18:19] offset:512 nt
	global_load_dwordx4 v[60:63], v136, s[18:19] offset:640 nt
	global_load_dwordx4 v[64:67], v136, s[18:19] offset:768 nt
	global_load_dwordx4 v[68:71], v136, s[18:19] offset:896 nt
	s_add_u32 s20, s16, 0x4000
	s_addc_u32 s21, s17, 0
	global_load_dwordx4 v[72:75], v136, s[20:21] offset:0 nt
	global_load_dwordx4 v[76:79], v136, s[20:21] offset:128 nt
	global_load_dwordx4 v[80:83], v136, s[20:21] offset:256 nt
	global_load_dwordx4 v[84:87], v136, s[20:21] offset:384 nt
	global_load_dwordx4 v[88:91], v136, s[20:21] offset:512 nt
	global_load_dwordx4 v[92:95], v136, s[20:21] offset:640 nt
	global_load_dwordx4 v[96:99], v136, s[20:21] offset:768 nt
	global_load_dwordx4 v[100:103], v136, s[20:21] offset:896 nt
	s_add_u32 s22, s16, 0x6000
	s_addc_u32 s23, s17, 0
	global_load_dwordx4 v[104:107], v136, s[22:23] offset:0 nt
	global_load_dwordx4 v[108:111], v136, s[22:23] offset:128 nt
	global_load_dwordx4 v[112:115], v136, s[22:23] offset:256 nt
	global_load_dwordx4 v[116:119], v136, s[22:23] offset:384 nt
	global_load_dwordx4 v[120:123], v136, s[22:23] offset:512 nt
	global_load_dwordx4 v[124:127], v136, s[22:23] offset:640 nt
	global_load_dwordx4 v[128:131], v136, s[22:23] offset:768 nt
	global_load_dwordx4 v[132:135], v136, s[22:23] offset:896 nt
	s_lshl_b32 s14, s2, 13
	s_add_u32 s24, s8, s14
	s_addc_u32 s25, s9, 0
	s_add_u32 s26, s24, 0x1000
	s_addc_u32 s27, s25, 0
	s_lshl_b32 s14, s2, 7
	s_add_u32 s28, s10, s14
	s_addc_u32 s29, s11, 0
	s_cmp_lg_u32 s2, 0
	s_cbranch_scc1 .Lprep_noinit
	v_cmp_gt_u32_e32 vcc, 32, v0
	s_and_saveexec_b64 s[30:31], vcc
	v_lshlrev_b32_e32 v1, 7, v0
	v_add_u32_e32 v1, 0x300000, v1
	v_mov_b32_e32 v2, 0
	v_mov_b32_e32 v3, 0
	global_store_dwordx2 v1, v[2:3], s[8:9]
	v_cmp_eq_u32_e32 vcc, 0, v0
	s_and_b64 exec, exec, vcc
	global_store_dword v2, v2, s[12:13]
	s_or_b64 exec, exec, s[30:31]

_Z11center_mainPKfPKcS0_Pf:
	s_load_dwordx4 s[4:7], s[0:1], 0x0
	s_load_dwordx4 s[8:11], s[0:1], 0x10
	s_and_b32 s3, s2, 7
	s_lshr_b32 s12, s2, 3
	s_mov_b32 s30, s2
	v_lshrrev_b32_e32 v1, 6, v0
	v_and_b32_e32 v2, 63, v0
	v_bfe_u32 v3, v0, 3, 3
	v_and_b32_e32 v4, 7, v0
	v_lshrrev_b32_e32 v5, 7, v0
	v_bfe_u32 v6, v0, 6, 1
	v_lshl_or_b32 v7, v5, 3, v3
	v_lshlrev_b32_e32 v8, 10, v7
	v_lshl_or_b32 v8, v6, 9, v8
	v_lshl_or_b32 v226, v4, 4, v8
	v_lshlrev_b32_e32 v17, 15, v1
	v_lshl_or_b32 v227, v2, 5, v17
	v_lshlrev_b32_e32 v237, 3, v0
	s_lshl_b32 s13, s3, 22
	s_lshl_b32 s14, s12, 15
	s_add_u32 s13, s13, s14
	s_lshl_b32 s15, s3, 18
	s_lshl_b32 s28, s3, 12
	s_waitcnt lgkmcnt(0)
	s_add_u32 s16, s4, s13
	s_addc_u32 s17, s5, 0
	global_load_dwordx4 v[194:197], v226, s[16:17] offset:0 nt
	global_load_dwordx4 v[198:201], v226, s[16:17] offset:128 nt
	global_load_dwordx4 v[202:205], v226, s[16:17] offset:256 nt
	global_load_dwordx4 v[206:209], v226, s[16:17] offset:384 nt
	s_add_u32 s8, s8, s28
	s_addc_u32 s9, s9, 0
	global_load_dwordx2 v[238:239], v237, s[8:9]
	s_add_u32 s24, s6, s15
	s_addc_u32 s25, s7, 0
	s_add_u32 s32, s24, 0x1000
	s_addc_u32 s33, s25, 0
	s_add_u32 s34, s24, 0x2000
	s_addc_u32 s35, s25, 0
	s_add_u32 s36, s24, 0x3000
	s_addc_u32 s37, s25, 0
	s_add_u32 s38, s24, 0x4000
	s_addc_u32 s39, s25, 0
	s_add_u32 s40, s24, 0x5000
	s_addc_u32 s41, s25, 0
	s_add_u32 s42, s24, 0x6000
	s_addc_u32 s43, s25, 0
	s_add_u32 s44, s24, 0x7000
	s_addc_u32 s45, s25, 0
	global_load_dwordx4 v[34:37], v227, s[24:25] offset:0
	global_load_dwordx4 v[38:41], v227, s[24:25] offset:16
	global_load_dwordx4 v[26:29], v227, s[24:25] offset:2048
	global_load_dwordx4 v[30:33], v227, s[24:25] offset:2064
	global_load_dwordx4 v[50:53], v227, s[32:33] offset:0
	global_load_dwordx4 v[54:57], v227, s[32:33] offset:16
	global_load_dwordx4 v[42:45], v227, s[32:33] offset:2048
	global_load_dwordx4 v[46:49], v227, s[32:33] offset:2064
	global_load_dwordx4 v[18:21], v227, s[34:35] offset:0
	global_load_dwordx4 v[22:25], v227, s[34:35] offset:16
	global_load_dwordx4 v[130:133], v227, s[34:35] offset:2048
	global_load_dwordx4 v[134:137], v227, s[34:35] offset:2064
	global_load_dwordx4 v[122:125], v227, s[36:37] offset:0
	global_load_dwordx4 v[126:129], v227, s[36:37] offset:16
	global_load_dwordx4 v[138:141], v227, s[36:37] offset:2048
	global_load_dwordx4 v[142:145], v227, s[36:37] offset:2064
	global_load_dwordx4 v[98:101], v227, s[38:39] offset:0
	global_load_dwordx4 v[102:105], v227, s[38:39] offset:16
	global_load_dwordx4 v[90:93], v227, s[38:39] offset:2048
	global_load_dwordx4 v[94:97], v227, s[38:39] offset:2064
	global_load_dwordx4 v[114:117], v227, s[40:41] offset:0
	global_load_dwordx4 v[118:121], v227, s[40:41] offset:16
	global_load_dwordx4 v[106:109], v227, s[40:41] offset:2048
	global_load_dwordx4 v[110:113], v227, s[40:41] offset:2064
	global_load_dwordx4 v[58:61], v227, s[42:43] offset:0
	global_load_dwordx4 v[62:65], v227, s[42:43] offset:16
	global_load_dwordx4 v[66:69], v227, s[42:43] offset:2048
	global_load_dwordx4 v[70:73], v227, s[42:43] offset:2064
	global_load_dwordx4 v[74:77], v227, s[44:45] offset:0
	global_load_dwordx4 v[78:81], v227, s[44:45] offset:16
	global_load_dwordx4 v[82:85], v227, s[44:45] offset:2048
	global_load_dwordx4 v[86:89], v227, s[44:45] offset:2064
	s_add_u32 s18, s16, 0x100000
	s_addc_u32 s19, s17, 0
	s_add_u32 s20, s16, 0x200000
	s_addc_u32 s21, s17, 0
	s_add_u32 s22, s16, 0x300000
	s_addc_u32 s23, s17, 0
	v_mul_u32_u24_e32 v9, 0x110, v7
	v_lshl_add_u32 v9, v6, 7, v9
	v_lshl_add_u32 v228, v4, 4, v9
	v_lshlrev_b32_e32 v10, 6, v7
	v_lshl_or_b32 v10, v6, 5, v10
	v_lshl_or_b32 v229, v4, 2, v10
	v_and_b32_e32 v11, 31, v0
	v_bfe_u32 v12, v0, 5, 1
	v_mul_u32_u24_e32 v13, 0x110, v11
	v_lshl_add_u32 v230, v12, 5, v13
	v_lshlrev_b32_e32 v14, 9, v1
	v_lshl_or_b32 v231, v12, 4, v14
	v_xor_b32_e32 v15, 32, v2
	v_lshlrev_b32_e32 v232, 2, v15
	v_xor_b32_e32 v15, 16, v2
	v_lshlrev_b32_e32 v247, 2, v15
	v_lshlrev_b32_e32 v16, 7, v1
	v_lshl_or_b32 v233, v11, 2, v16
	v_mov_b32_e32 v234, 0x7f7f7f7f
	s_waitcnt vmcnt(32)
	ds_write_b64 v237, v[238:239] offset:34816
	v_mul_f32_e32 v244, v194, v194
	v_mul_f32_e32 v245, v198, v198
	v_cvt_pk_fp8_f32 v240, v194, v195
	v_cvt_pk_fp8_f32 v241, v198, v199
	v_cvt_pk_fp8_f32 v242, v202, v203
	v_cvt_pk_fp8_f32 v243, v206, v207
	v_fmac_f32_e32 v244, v195, v195
	v_fmac_f32_e32 v245, v199, v199
	v_fmac_f32_e32 v244, v196, v196
	v_fmac_f32_e32 v245, v200, v200
	v_fmac_f32_e32 v244, v197, v197
	v_fmac_f32_e32 v245, v201, v201
	v_fmac_f32_e32 v244, v202, v202
	v_fmac_f32_e32 v245, v206, v206
	v_fmac_f32_e32 v244, v203, v203
	v_fmac_f32_e32 v245, v207, v207
	v_fmac_f32_e32 v244, v204, v204
	v_fmac_f32_e32 v245, v208, v208
	v_fmac_f32_e32 v244, v205, v205
	v_fmac_f32_e32 v245, v209, v209
	v_cvt_pk_fp8_f32 v240, v196, v197 op_sel:[0,0,1]
	v_cvt_pk_fp8_f32 v241, v200, v201 op_sel:[0,0,1]
	v_cvt_pk_fp8_f32 v242, v204, v205 op_sel:[0,0,1]
	v_cvt_pk_fp8_f32 v243, v208, v209 op_sel:[0,0,1]
	v_add_f32_e32 v244, v244, v245
	s_nop 0
	ds_write_b128 v228, v[240:243] offset:0
	ds_write_b32 v229, v244 offset:38912
	global_load_dwordx4 v[210:213], v226, s[18:19] offset:0 nt
	global_load_dwordx4 v[214:217], v226, s[18:19] offset:128 nt
	global_load_dwordx4 v[218:221], v226, s[18:19] offset:256 nt
	global_load_dwordx4 v[222:225], v226, s[18:19] offset:384 nt
	s_waitcnt lgkmcnt(0)
	s_barrier
	ds_read_b128 v[162:165], v230 offset:0
	ds_read_b128 v[166:169], v230 offset:16
	ds_read_b128 v[2:5], v231 offset:34816
	ds_read_b128 v[6:9], v231 offset:34848
	ds_read_b128 v[10:13], v231 offset:34880
	ds_read_b128 v[14:17], v231 offset:34912
	ds_read_b128 v[170:173], v230 offset:64
	ds_read_b128 v[174:177], v230 offset:80
	ds_read_b128 v[178:181], v230 offset:128
	ds_read_b128 v[182:185], v230 offset:144
	ds_read_b128 v[186:189], v230 offset:192
	ds_read_b128 v[190:193], v230 offset:208
	s_waitcnt vmcnt(34) lgkmcnt(6)
	v_mfma_scale_f32_32x32x64_f8f6f4 v[2:17], v[34:41], v[162:169], v[2:17], v234, v234 op_sel_hi:[0,0,0]
	s_waitcnt vmcnt(32) lgkmcnt(4)
	v_mfma_scale_f32_32x32x64_f8f6f4 v[2:17], v[26:33], v[170:177], v[2:17], v234, v234 op_sel_hi:[0,0,0]
	s_waitcnt vmcnt(30) lgkmcnt(2)
	v_mfma_scale_f32_32x32x64_f8f6f4 v[2:17], v[50:57], v[178:185], v[2:17], v234, v234 op_sel_hi:[0,0,0]
	s_waitcnt vmcnt(28) lgkmcnt(0)
	v_mfma_scale_f32_32x32x64_f8f6f4 v[2:17], v[42:49], v[186:193], v[2:17], v234, v234 op_sel_hi:[0,0,0]
	ds_read_b128 v[146:149], v231 offset:34944
	ds_read_b128 v[150:153], v231 offset:34976
	ds_read_b128 v[154:157], v231 offset:35008
	ds_read_b128 v[158:161], v231 offset:35040
	s_waitcnt vmcnt(26) lgkmcnt(0)
	v_mfma_scale_f32_32x32x64_f8f6f4 v[146:161], v[18:25], v[162:169], v[146:161], v234, v234 op_sel_hi:[0,0,0]
	s_waitcnt vmcnt(24)
	v_mfma_scale_f32_32x32x64_f8f6f4 v[146:161], v[130:137], v[170:177], v[146:161], v234, v234 op_sel_hi:[0,0,0]
	s_waitcnt vmcnt(22)
	v_mfma_scale_f32_32x32x64_f8f6f4 v[146:161], v[122:129], v[178:185], v[146:161], v234, v234 op_sel_hi:[0,0,0]
	s_waitcnt vmcnt(20)
	v_mfma_scale_f32_32x32x64_f8f6f4 v[146:161], v[138:145], v[186:193], v[146:161], v234, v234 op_sel_hi:[0,0,0]
	s_nop 15
	v_min3_f32 v2, v2, v3, v4
	v_min3_f32 v5, v5, v6, v7
	v_min3_f32 v8, v8, v9, v10
	v_min3_f32 v11, v11, v12, v13
	v_min3_f32 v14, v14, v15, v16
	v_min3_f32 v2, v2, v5, v8
	v_min3_f32 v11, v11, v14, v17
	v_min_f32_e32 v235, v2, v11
	ds_read_b128 v[2:5], v231 offset:35072
	ds_read_b128 v[6:9], v231 offset:35104
	ds_read_b128 v[10:13], v231 offset:35136
	ds_read_b128 v[14:17], v231 offset:35168
	s_waitcnt vmcnt(18) lgkmcnt(0)
	v_mfma_scale_f32_32x32x64_f8f6f4 v[2:17], v[98:105], v[162:169], v[2:17], v234, v234 op_sel_hi:[0,0,0]
	s_waitcnt vmcnt(16)
	v_mfma_scale_f32_32x32x64_f8f6f4 v[2:17], v[90:97], v[170:177], v[2:17], v234, v234 op_sel_hi:[0,0,0]
	s_waitcnt vmcnt(14)
	v_mfma_scale_f32_32x32x64_f8f6f4 v[2:17], v[114:121], v[178:185], v[2:17], v234, v234 op_sel_hi:[0,0,0]
	s_waitcnt vmcnt(12)
	v_mfma_scale_f32_32x32x64_f8f6f4 v[2:17], v[106:113], v[186:193], v[2:17], v234, v234 op_sel_hi:[0,0,0]
	s_nop 15
	v_min3_f32 v146, v146, v147, v148
	v_min3_f32 v149, v149, v150, v151
	v_min3_f32 v152, v152, v153, v154
	v_min3_f32 v155, v155, v156, v157
	v_min3_f32 v158, v158, v159, v160
	v_min3_f32 v146, v146, v149, v152
	v_min3_f32 v155, v155, v158, v161
	v_min3_f32 v235, v235, v146, v155
	ds_read_b128 v[146:149], v231 offset:35200
	ds_read_b128 v[150:153], v231 offset:35232
	ds_read_b128 v[154:157], v231 offset:35264
	ds_read_b128 v[158:161], v231 offset:35296
	s_waitcnt vmcnt(10) lgkmcnt(0)
	v_mfma_scale_f32_32x32x64_f8f6f4 v[146:161], v[58:65], v[162:169], v[146:161], v234, v234 op_sel_hi:[0,0,0]
	s_waitcnt vmcnt(8)
	v_mfma_scale_f32_32x32x64_f8f6f4 v[146:161], v[66:73], v[170:177], v[146:161], v234, v234 op_sel_hi:[0,0,0]
	s_waitcnt vmcnt(6)
	v_mfma_scale_f32_32x32x64_f8f6f4 v[146:161], v[74:81], v[178:185], v[146:161], v234, v234 op_sel_hi:[0,0,0]
	s_waitcnt vmcnt(4)
	v_mfma_scale_f32_32x32x64_f8f6f4 v[146:161], v[82:89], v[186:193], v[146:161], v234, v234 op_sel_hi:[0,0,0]
	global_load_dwordx4 v[194:197], v226, s[20:21] offset:0 nt
	global_load_dwordx4 v[198:201], v226, s[20:21] offset:128 nt
	global_load_dwordx4 v[202:205], v226, s[20:21] offset:256 nt
	global_load_dwordx4 v[206:209], v226, s[20:21] offset:384 nt
	s_waitcnt vmcnt(4)
	v_mul_f32_e32 v244, v210, v210
	v_mul_f32_e32 v245, v214, v214
	v_cvt_pk_fp8_f32 v240, v210, v211
	v_cvt_pk_fp8_f32 v241, v214, v215
	v_cvt_pk_fp8_f32 v242, v218, v219
	v_cvt_pk_fp8_f32 v243, v222, v223
	v_fmac_f32_e32 v244, v211, v211
	v_fmac_f32_e32 v245, v215, v215
	v_fmac_f32_e32 v244, v212, v212
	v_fmac_f32_e32 v245, v216, v216
	v_fmac_f32_e32 v244, v213, v213
	v_fmac_f32_e32 v245, v217, v217
	v_fmac_f32_e32 v244, v218, v218
	v_fmac_f32_e32 v245, v222, v222
	v_fmac_f32_e32 v244, v219, v219
	v_fmac_f32_e32 v245, v223, v223
	v_fmac_f32_e32 v244, v220, v220
	v_fmac_f32_e32 v245, v224, v224
	v_fmac_f32_e32 v244, v221, v221
	v_fmac_f32_e32 v245, v225, v225
	v_cvt_pk_fp8_f32 v240, v212, v213 op_sel:[0,0,1]
	v_cvt_pk_fp8_f32 v241, v216, v217 op_sel:[0,0,1]
	v_cvt_pk_fp8_f32 v242, v220, v221 op_sel:[0,0,1]
	v_cvt_pk_fp8_f32 v243, v224, v225 op_sel:[0,0,1]
	v_add_f32_e32 v244, v244, v245
	s_nop 0
	ds_write_b128 v228, v[240:243] offset:8704
	ds_write_b32 v229, v244 offset:40960
	v_min3_f32 v2, v2, v3, v4
	v_min3_f32 v5, v5, v6, v7
	v_min3_f32 v8, v8, v9, v10
	v_min3_f32 v11, v11, v12, v13
	v_min3_f32 v14, v14, v15, v16
	v_min3_f32 v2, v2, v5, v8
	v_min3_f32 v11, v11, v14, v17
	v_min3_f32 v235, v235, v2, v11
	ds_read_b128 v[2:5], v231 offset:34816
	ds_read_b128 v[6:9], v231 offset:34848
	ds_read_b128 v[10:13], v231 offset:34880
	ds_read_b128 v[14:17], v231 offset:34912
	s_waitcnt lgkmcnt(0)
	s_barrier
	ds_read_b128 v[162:165], v230 offset:8704
	ds_read_b128 v[166:169], v230 offset:8720
	ds_read_b128 v[170:173], v230 offset:8768
	ds_read_b128 v[174:177], v230 offset:8784
	ds_read_b128 v[178:181], v230 offset:8832
	ds_read_b128 v[182:185], v230 offset:8848
	ds_read_b128 v[186:189], v230 offset:8896
	ds_read_b128 v[190:193], v230 offset:8912
	s_waitcnt lgkmcnt(6)
	v_mfma_scale_f32_32x32x64_f8f6f4 v[2:17], v[34:41], v[162:169], v[2:17], v234, v234 op_sel_hi:[0,0,0]
	s_waitcnt lgkmcnt(4)
	v_mfma_scale_f32_32x32x64_f8f6f4 v[2:17], v[26:33], v[170:177], v[2:17], v234, v234 op_sel_hi:[0,0,0]
	s_waitcnt lgkmcnt(2)
	v_mfma_scale_f32_32x32x64_f8f6f4 v[2:17], v[50:57], v[178:185], v[2:17], v234, v234 op_sel_hi:[0,0,0]
	s_waitcnt lgkmcnt(0)
	v_mfma_scale_f32_32x32x64_f8f6f4 v[2:17], v[42:49], v[186:193], v[2:17], v234, v234 op_sel_hi:[0,0,0]
	s_nop 15
	v_min3_f32 v146, v146, v147, v148
	v_min3_f32 v149, v149, v150, v151
	v_min3_f32 v152, v152, v153, v154
	v_min3_f32 v155, v155, v156, v157
	v_min3_f32 v158, v158, v159, v160
	v_min3_f32 v146, v146, v149, v152
	v_min3_f32 v155, v155, v158, v161
	v_min3_f32 v235, v235, v146, v155
	ds_bpermute_b32 v246, v232, v235
	s_waitcnt lgkmcnt(0)
	v_min_f32_e32 v246, v235, v246
	ds_write_b32 v233, v246 offset:47104
	ds_read_b128 v[146:149], v231 offset:34944
	ds_read_b128 v[150:153], v231 offset:34976
	ds_read_b128 v[154:157], v231 offset:35008
	ds_read_b128 v[158:161], v231 offset:35040
	s_waitcnt lgkmcnt(0)
	v_mfma_scale_f32_32x32x64_f8f6f4 v[146:161], v[18:25], v[162:169], v[146:161], v234, v234 op_sel_hi:[0,0,0]
	v_mfma_scale_f32_32x32x64_f8f6f4 v[146:161], v[130:137], v[170:177], v[146:161], v234, v234 op_sel_hi:[0,0,0]
	v_mfma_scale_f32_32x32x64_f8f6f4 v[146:161], v[122:129], v[178:185], v[146:161], v234, v234 op_sel_hi:[0,0,0]
	v_mfma_scale_f32_32x32x64_f8f6f4 v[146:161], v[138:145], v[186:193], v[146:161], v234, v234 op_sel_hi:[0,0,0]
	s_nop 15
	v_min3_f32 v2, v2, v3, v4
	v_min3_f32 v5, v5, v6, v7
	v_min3_f32 v8, v8, v9, v10
	v_min3_f32 v11, v11, v12, v13
	v_min3_f32 v14, v14, v15, v16
	v_min3_f32 v2, v2, v5, v8
	v_min3_f32 v11, v11, v14, v17
	v_min_f32_e32 v236, v2, v11
	ds_read_b128 v[2:5], v231 offset:35072
	ds_read_b128 v[6:9], v231 offset:35104
	ds_read_b128 v[10:13], v231 offset:35136
	ds_read_b128 v[14:17], v231 offset:35168
	s_waitcnt lgkmcnt(0)
	v_mfma_scale_f32_32x32x64_f8f6f4 v[2:17], v[98:105], v[162:169], v[2:17], v234, v234 op_sel_hi:[0,0,0]
	v_mfma_scale_f32_32x32x64_f8f6f4 v[2:17], v[90:97], v[170:177], v[2:17], v234, v234 op_sel_hi:[0,0,0]
	v_mfma_scale_f32_32x32x64_f8f6f4 v[2:17], v[114:121], v[178:185], v[2:17], v234, v234 op_sel_hi:[0,0,0]
	v_mfma_scale_f32_32x32x64_f8f6f4 v[2:17], v[106:113], v[186:193], v[2:17], v234, v234 op_sel_hi:[0,0,0]
	s_nop 15
	v_min3_f32 v146, v146, v147, v148
	v_min3_f32 v149, v149, v150, v151
	v_min3_f32 v152, v152, v153, v154
	v_min3_f32 v155, v155, v156, v157
	v_min3_f32 v158, v158, v159, v160
	v_min3_f32 v146, v146, v149, v152
	v_min3_f32 v155, v155, v158, v161
	v_min3_f32 v236, v236, v146, v155
	ds_read_b128 v[146:149], v231 offset:35200
	ds_read_b128 v[150:153], v231 offset:35232
	ds_read_b128 v[154:157], v231 offset:35264
	ds_read_b128 v[158:161], v231 offset:35296
	s_waitcnt lgkmcnt(0)
	v_mfma_scale_f32_32x32x64_f8f6f4 v[146:161], v[58:65], v[162:169], v[146:161], v234, v234 op_sel_hi:[0,0,0]
	v_mfma_scale_f32_32x32x64_f8f6f4 v[146:161], v[66:73], v[170:177], v[146:161], v234, v234 op_sel_hi:[0,0,0]
	v_mfma_scale_f32_32x32x64_f8f6f4 v[146:161], v[74:81], v[178:185], v[146:161], v234, v234 op_sel_hi:[0,0,0]
	v_mfma_scale_f32_32x32x64_f8f6f4 v[146:161], v[82:89], v[186:193], v[146:161], v234, v234 op_sel_hi:[0,0,0]
	global_load_dwordx4 v[210:213], v226, s[22:23] offset:0 nt
	global_load_dwordx4 v[214:217], v226, s[22:23] offset:128 nt
	global_load_dwordx4 v[218:221], v226, s[22:23] offset:256 nt
	global_load_dwordx4 v[222:225], v226, s[22:23] offset:384 nt
	s_waitcnt vmcnt(4)
	v_mul_f32_e32 v244, v194, v194
	v_mul_f32_e32 v245, v198, v198
	v_cvt_pk_fp8_f32 v240, v194, v195
	v_cvt_pk_fp8_f32 v241, v198, v199
	v_cvt_pk_fp8_f32 v242, v202, v203
	v_cvt_pk_fp8_f32 v243, v206, v207
	v_fmac_f32_e32 v244, v195, v195
	v_fmac_f32_e32 v245, v199, v199
	v_fmac_f32_e32 v244, v196, v196
	v_fmac_f32_e32 v245, v200, v200
	v_fmac_f32_e32 v244, v197, v197
	v_fmac_f32_e32 v245, v201, v201
	v_fmac_f32_e32 v244, v202, v202
	v_fmac_f32_e32 v245, v206, v206
	v_fmac_f32_e32 v244, v203, v203
	v_fmac_f32_e32 v245, v207, v207
	v_fmac_f32_e32 v244, v204, v204
	v_fmac_f32_e32 v245, v208, v208
	v_fmac_f32_e32 v244, v205, v205
	v_fmac_f32_e32 v245, v209, v209
	v_cvt_pk_fp8_f32 v240, v196, v197 op_sel:[0,0,1]
	v_cvt_pk_fp8_f32 v241, v200, v201 op_sel:[0,0,1]
	v_cvt_pk_fp8_f32 v242, v204, v205 op_sel:[0,0,1]
	v_cvt_pk_fp8_f32 v243, v208, v209 op_sel:[0,0,1]
	v_add_f32_e32 v244, v244, v245
	s_nop 0
	ds_write_b128 v228, v[240:243] offset:17408
	ds_write_b32 v229, v244 offset:43008
	v_min3_f32 v2, v2, v3, v4
	v_min3_f32 v5, v5, v6, v7
	v_min3_f32 v8, v8, v9, v10
	v_min3_f32 v11, v11, v12, v13
	v_min3_f32 v14, v14, v15, v16
	v_min3_f32 v2, v2, v5, v8
	v_min3_f32 v11, v11, v14, v17
	v_min3_f32 v236, v236, v2, v11
	ds_read_b128 v[2:5], v231 offset:34816
	ds_read_b128 v[6:9], v231 offset:34848
	ds_read_b128 v[10:13], v231 offset:34880
	ds_read_b128 v[14:17], v231 offset:34912
	s_waitcnt lgkmcnt(0)
	s_barrier
	ds_read_b128 v[162:165], v230 offset:17408
	ds_read_b128 v[166:169], v230 offset:17424
	ds_read_b128 v[170:173], v230 offset:17472
	ds_read_b128 v[174:177], v230 offset:17488
	ds_read_b128 v[178:181], v230 offset:17536
	ds_read_b128 v[182:185], v230 offset:17552
	ds_read_b128 v[186:189], v230 offset:17600
	ds_read_b128 v[190:193], v230 offset:17616
	s_waitcnt lgkmcnt(6)
	v_mfma_scale_f32_32x32x64_f8f6f4 v[2:17], v[34:41], v[162:169], v[2:17], v234, v234 op_sel_hi:[0,0,0]
	s_waitcnt lgkmcnt(4)
	v_mfma_scale_f32_32x32x64_f8f6f4 v[2:17], v[26:33], v[170:177], v[2:17], v234, v234 op_sel_hi:[0,0,0]
	s_waitcnt lgkmcnt(2)
	v_mfma_scale_f32_32x32x64_f8f6f4 v[2:17], v[50:57], v[178:185], v[2:17], v234, v234 op_sel_hi:[0,0,0]
	s_waitcnt lgkmcnt(0)
	v_mfma_scale_f32_32x32x64_f8f6f4 v[2:17], v[42:49], v[186:193], v[2:17], v234, v234 op_sel_hi:[0,0,0]
	s_nop 15
	v_min3_f32 v146, v146, v147, v148
	v_min3_f32 v149, v149, v150, v151
	v_min3_f32 v152, v152, v153, v154
	v_min3_f32 v155, v155, v156, v157
	v_min3_f32 v158, v158, v159, v160
	v_min3_f32 v146, v146, v149, v152
	v_min3_f32 v155, v155, v158, v161
	v_min3_f32 v236, v236, v146, v155
	ds_bpermute_b32 v246, v232, v236
	s_waitcnt lgkmcnt(0)
	v_min_f32_e32 v246, v236, v246
	ds_write_b32 v233, v246 offset:48128
	ds_read_b128 v[146:149], v231 offset:34944
	ds_read_b128 v[150:153], v231 offset:34976
	ds_read_b128 v[154:157], v231 offset:35008
	ds_read_b128 v[158:161], v231 offset:35040
	s_waitcnt lgkmcnt(0)
	v_mfma_scale_f32_32x32x64_f8f6f4 v[146:161], v[18:25], v[162:169], v[146:161], v234, v234 op_sel_hi:[0,0,0]
	v_mfma_scale_f32_32x32x64_f8f6f4 v[146:161], v[130:137], v[170:177], v[146:161], v234, v234 op_sel_hi:[0,0,0]
	v_mfma_scale_f32_32x32x64_f8f6f4 v[146:161], v[122:129], v[178:185], v[146:161], v234, v234 op_sel_hi:[0,0,0]
	v_mfma_scale_f32_32x32x64_f8f6f4 v[146:161], v[138:145], v[186:193], v[146:161], v234, v234 op_sel_hi:[0,0,0]
	s_nop 15
	v_min3_f32 v2, v2, v3, v4
	v_min3_f32 v5, v5, v6, v7
	v_min3_f32 v8, v8, v9, v10
	v_min3_f32 v11, v11, v12, v13
	v_min3_f32 v14, v14, v15, v16
	v_min3_f32 v2, v2, v5, v8
	v_min3_f32 v11, v11, v14, v17
	v_min_f32_e32 v235, v2, v11
	ds_read_b128 v[2:5], v231 offset:35072
	ds_read_b128 v[6:9], v231 offset:35104
	ds_read_b128 v[10:13], v231 offset:35136
	ds_read_b128 v[14:17], v231 offset:35168
	s_waitcnt lgkmcnt(0)
	v_mfma_scale_f32_32x32x64_f8f6f4 v[2:17], v[98:105], v[162:169], v[2:17], v234, v234 op_sel_hi:[0,0,0]
	v_mfma_scale_f32_32x32x64_f8f6f4 v[2:17], v[90:97], v[170:177], v[2:17], v234, v234 op_sel_hi:[0,0,0]
	v_mfma_scale_f32_32x32x64_f8f6f4 v[2:17], v[114:121], v[178:185], v[2:17], v234, v234 op_sel_hi:[0,0,0]
	v_mfma_scale_f32_32x32x64_f8f6f4 v[2:17], v[106:113], v[186:193], v[2:17], v234, v234 op_sel_hi:[0,0,0]
	s_nop 15
	v_min3_f32 v146, v146, v147, v148
	v_min3_f32 v149, v149, v150, v151
	v_min3_f32 v152, v152, v153, v154
	v_min3_f32 v155, v155, v156, v157
	v_min3_f32 v158, v158, v159, v160
	v_min3_f32 v146, v146, v149, v152
	v_min3_f32 v155, v155, v158, v161
	v_min3_f32 v235, v235, v146, v155
	ds_read_b128 v[146:149], v231 offset:35200
	ds_read_b128 v[150:153], v231 offset:35232
	ds_read_b128 v[154:157], v231 offset:35264
	ds_read_b128 v[158:161], v231 offset:35296
	s_waitcnt lgkmcnt(0)
	v_mfma_scale_f32_32x32x64_f8f6f4 v[146:161], v[58:65], v[162:169], v[146:161], v234, v234 op_sel_hi:[0,0,0]
	v_mfma_scale_f32_32x32x64_f8f6f4 v[146:161], v[66:73], v[170:177], v[146:161], v234, v234 op_sel_hi:[0,0,0]
	v_mfma_scale_f32_32x32x64_f8f6f4 v[146:161], v[74:81], v[178:185], v[146:161], v234, v234 op_sel_hi:[0,0,0]
	v_mfma_scale_f32_32x32x64_f8f6f4 v[146:161], v[82:89], v[186:193], v[146:161], v234, v234 op_sel_hi:[0,0,0]
	s_waitcnt vmcnt(0)
	v_mul_f32_e32 v244, v210, v210
	v_mul_f32_e32 v245, v214, v214
	v_cvt_pk_fp8_f32 v240, v210, v211
	v_cvt_pk_fp8_f32 v241, v214, v215
	v_cvt_pk_fp8_f32 v242, v218, v219
	v_cvt_pk_fp8_f32 v243, v222, v223
	v_fmac_f32_e32 v244, v211, v211
	v_fmac_f32_e32 v245, v215, v215
	v_fmac_f32_e32 v244, v212, v212
	v_fmac_f32_e32 v245, v216, v216
	v_fmac_f32_e32 v244, v213, v213
	v_fmac_f32_e32 v245, v217, v217
	v_fmac_f32_e32 v244, v218, v218
	v_fmac_f32_e32 v245, v222, v222
	v_fmac_f32_e32 v244, v219, v219
	v_fmac_f32_e32 v245, v223, v223
	v_fmac_f32_e32 v244, v220, v220
	v_fmac_f32_e32 v245, v224, v224
	v_fmac_f32_e32 v244, v221, v221
	v_fmac_f32_e32 v245, v225, v225
	v_cvt_pk_fp8_f32 v240, v212, v213 op_sel:[0,0,1]
	v_cvt_pk_fp8_f32 v241, v216, v217 op_sel:[0,0,1]
	v_cvt_pk_fp8_f32 v242, v220, v221 op_sel:[0,0,1]
	v_cvt_pk_fp8_f32 v243, v224, v225 op_sel:[0,0,1]
	v_add_f32_e32 v244, v244, v245
	s_nop 0
	ds_write_b128 v228, v[240:243] offset:26112
	ds_write_b32 v229, v244 offset:45056
	v_min3_f32 v2, v2, v3, v4
	v_min3_f32 v5, v5, v6, v7
	v_min3_f32 v8, v8, v9, v10
	v_min3_f32 v11, v11, v12, v13
	v_min3_f32 v14, v14, v15, v16
	v_min3_f32 v2, v2, v5, v8
	v_min3_f32 v11, v11, v14, v17
	v_min3_f32 v235, v235, v2, v11
	ds_read_b128 v[2:5], v231 offset:34816
	ds_read_b128 v[6:9], v231 offset:34848
	ds_read_b128 v[10:13], v231 offset:34880
	ds_read_b128 v[14:17], v231 offset:34912
	s_waitcnt lgkmcnt(0)
	s_barrier
	ds_read_b128 v[162:165], v230 offset:26112
	ds_read_b128 v[166:169], v230 offset:26128
	ds_read_b128 v[170:173], v230 offset:26176
	ds_read_b128 v[174:177], v230 offset:26192
	ds_read_b128 v[178:181], v230 offset:26240
	ds_read_b128 v[182:185], v230 offset:26256
	ds_read_b128 v[186:189], v230 offset:26304
	ds_read_b128 v[190:193], v230 offset:26320
	s_waitcnt lgkmcnt(6)
	v_mfma_scale_f32_32x32x64_f8f6f4 v[2:17], v[34:41], v[162:169], v[2:17], v234, v234 op_sel_hi:[0,0,0]
	s_waitcnt lgkmcnt(4)
	v_mfma_scale_f32_32x32x64_f8f6f4 v[2:17], v[26:33], v[170:177], v[2:17], v234, v234 op_sel_hi:[0,0,0]
	s_waitcnt lgkmcnt(2)
	v_mfma_scale_f32_32x32x64_f8f6f4 v[2:17], v[50:57], v[178:185], v[2:17], v234, v234 op_sel_hi:[0,0,0]
	s_waitcnt lgkmcnt(0)
	v_mfma_scale_f32_32x32x64_f8f6f4 v[2:17], v[42:49], v[186:193], v[2:17], v234, v234 op_sel_hi:[0,0,0]
	s_nop 15
	v_min3_f32 v146, v146, v147, v148
	v_min3_f32 v149, v149, v150, v151
	v_min3_f32 v152, v152, v153, v154
	v_min3_f32 v155, v155, v156, v157
	v_min3_f32 v158, v158, v159, v160
	v_min3_f32 v146, v146, v149, v152
	v_min3_f32 v155, v155, v158, v161
	v_min3_f32 v235, v235, v146, v155
	ds_bpermute_b32 v246, v232, v235
	s_waitcnt lgkmcnt(0)
	v_min_f32_e32 v246, v235, v246
	ds_write_b32 v233, v246 offset:49152
	ds_read_b128 v[146:149], v231 offset:34944
	ds_read_b128 v[150:153], v231 offset:34976
	ds_read_b128 v[154:157], v231 offset:35008
	ds_read_b128 v[158:161], v231 offset:35040
	s_waitcnt lgkmcnt(0)
	v_mfma_scale_f32_32x32x64_f8f6f4 v[146:161], v[18:25], v[162:169], v[146:161], v234, v234 op_sel_hi:[0,0,0]
	v_mfma_scale_f32_32x32x64_f8f6f4 v[146:161], v[130:137], v[170:177], v[146:161], v234, v234 op_sel_hi:[0,0,0]
	v_mfma_scale_f32_32x32x64_f8f6f4 v[146:161], v[122:129], v[178:185], v[146:161], v234, v234 op_sel_hi:[0,0,0]
	v_mfma_scale_f32_32x32x64_f8f6f4 v[146:161], v[138:145], v[186:193], v[146:161], v234, v234 op_sel_hi:[0,0,0]
	s_nop 15
	v_min3_f32 v2, v2, v3, v4
	v_min3_f32 v5, v5, v6, v7
	v_min3_f32 v8, v8, v9, v10
	v_min3_f32 v11, v11, v12, v13
	v_min3_f32 v14, v14, v15, v16
	v_min3_f32 v2, v2, v5, v8
	v_min3_f32 v11, v11, v14, v17
	v_min_f32_e32 v236, v2, v11
	ds_read_b128 v[2:5], v231 offset:35072
	ds_read_b128 v[6:9], v231 offset:35104
	ds_read_b128 v[10:13], v231 offset:35136
	ds_read_b128 v[14:17], v231 offset:35168
	s_waitcnt lgkmcnt(0)
	v_mfma_scale_f32_32x32x64_f8f6f4 v[2:17], v[98:105], v[162:169], v[2:17], v234, v234 op_sel_hi:[0,0,0]
	v_mfma_scale_f32_32x32x64_f8f6f4 v[2:17], v[90:97], v[170:177], v[2:17], v234, v234 op_sel_hi:[0,0,0]
	v_mfma_scale_f32_32x32x64_f8f6f4 v[2:17], v[114:121], v[178:185], v[2:17], v234, v234 op_sel_hi:[0,0,0]
	v_mfma_scale_f32_32x32x64_f8f6f4 v[2:17], v[106:113], v[186:193], v[2:17], v234, v234 op_sel_hi:[0,0,0]
	s_nop 15
	v_min3_f32 v146, v146, v147, v148
	v_min3_f32 v149, v149, v150, v151
	v_min3_f32 v152, v152, v153, v154
	v_min3_f32 v155, v155, v156, v157
	v_min3_f32 v158, v158, v159, v160
	v_min3_f32 v146, v146, v149, v152
	v_min3_f32 v155, v155, v158, v161
	v_min3_f32 v236, v236, v146, v155
	ds_read_b128 v[146:149], v231 offset:35200
	ds_read_b128 v[150:153], v231 offset:35232
	ds_read_b128 v[154:157], v231 offset:35264
	ds_read_b128 v[158:161], v231 offset:35296
	s_waitcnt lgkmcnt(0)
	v_mfma_scale_f32_32x32x64_f8f6f4 v[146:161], v[58:65], v[162:169], v[146:161], v234, v234 op_sel_hi:[0,0,0]
	v_mfma_scale_f32_32x32x64_f8f6f4 v[146:161], v[66:73], v[170:177], v[146:161], v234, v234 op_sel_hi:[0,0,0]
	v_mfma_scale_f32_32x32x64_f8f6f4 v[146:161], v[74:81], v[178:185], v[146:161], v234, v234 op_sel_hi:[0,0,0]
	v_mfma_scale_f32_32x32x64_f8f6f4 v[146:161], v[82:89], v[186:193], v[146:161], v234, v234 op_sel_hi:[0,0,0]
	s_nop 15
	v_min3_f32 v2, v2, v3, v4
	v_min3_f32 v5, v5, v6, v7
	v_min3_f32 v8, v8, v9, v10
	v_min3_f32 v11, v11, v12, v13
	v_min3_f32 v14, v14, v15, v16
	v_min3_f32 v2, v2, v5, v8
	v_min3_f32 v11, v11, v14, v17
	v_min3_f32 v236, v236, v2, v11
	s_nop 15
	s_nop 3
	v_min3_f32 v146, v146, v147, v148
	v_min3_f32 v149, v149, v150, v151
	v_min3_f32 v152, v152, v153, v154
	v_min3_f32 v155, v155, v156, v157
	v_min3_f32 v158, v158, v159, v160
	v_min3_f32 v146, v146, v149, v152
	v_min3_f32 v155, v155, v158, v161
	v_min3_f32 v236, v236, v146, v155
	ds_bpermute_b32 v246, v232, v236
	s_waitcnt lgkmcnt(0)
	v_min_f32_e32 v246, v236, v246
	ds_write_b32 v233, v246 offset:50176
	s_waitcnt lgkmcnt(0)
	s_barrier
	v_readfirstlane_b32 s2, v1
	s_nop 3
	s_cmp_gt_u32 s2, 1
	s_cbranch_scc1 .Lmain_end
	v_and_b32_e32 v2, 31, v0
	v_lshlrev_b32_e32 v3, 5, v0
	v_and_b32_e32 v3, 0xc00, v3
	v_lshl_or_b32 v8, v2, 2, v3
	v_add_u32_e32 v8, 0xb800, v8
	v_lshlrev_b32_e32 v14, 6, v0
	ds_read2_b32 v[2:3], v8 offset1:32
	ds_read2_b32 v[4:5], v8 offset0:64 offset1:96
	ds_read2_b32 v[6:7], v8 offset0:128 offset1:160
	ds_read2_b32 v[10:11], v8 offset0:192 offset1:224
	ds_read_b128 v[20:23], v14 offset:38912
	ds_read_b128 v[24:27], v14 offset:38928
	ds_read_b128 v[28:31], v14 offset:38944
	ds_read_b128 v[32:35], v14 offset:38960
	s_mov_b32 s8, 0xf800000
	s_lshr_b32 s2, s30, 3
	s_lshl_b32 s2, s2, 7
	s_add_u32 s2, s2, 0x300000
	s_add_u32 s6, s6, s2
	s_addc_u32 s7, s7, 0
	s_mov_b32 s4, 0
	s_mov_b32 s5, 0x41d00000
	s_mov_b32 s16, 0
	s_mov_b32 s17, 0x420e0000
	s_waitcnt lgkmcnt(4)
	v_min3_f32 v2, v2, v3, v4
	v_min3_f32 v5, v5, v6, v7
	v_min3_f32 v2, v2, v10, v11
	v_min_f32_e32 v2, v2, v5
	s_waitcnt lgkmcnt(0)
	v_add_f32_e32 v20, v20, v21
	v_add_f32_e32 v22, v22, v23
	v_add_f32_e32 v24, v24, v25
	v_add_f32_e32 v26, v26, v27
	v_add_f32_e32 v28, v28, v29
	v_add_f32_e32 v30, v30, v31
	v_add_f32_e32 v32, v32, v33
	v_add_f32_e32 v34, v34, v35
	v_add_f32_e32 v20, v20, v22
	v_add_f32_e32 v24, v24, v26
	v_add_f32_e32 v28, v28, v30
	v_add_f32_e32 v32, v32, v34
	v_add_f32_e32 v20, v20, v24
	v_add_f32_e32 v28, v28, v32
	v_add_f32_e32 v20, v20, v28
	v_add_f32_e32 v2, v2, v20
	v_max_f32_e32 v2, 0, v2
	v_mul_f32_e32 v3, 0x4f800000, v2
	v_cmp_gt_f32_e32 vcc, s8, v2
	s_nop 1
	v_cndmask_b32_e32 v2, v2, v3, vcc
	v_sqrt_f32_e32 v3, v2
	s_nop 0
	v_add_u32_e32 v4, -1, v3
	v_fma_f32 v5, -v4, v3, v2
	v_cmp_ge_f32_e64 s[18:19], 0, v5
	v_add_u32_e32 v5, 1, v3
	s_nop 0
	v_cndmask_b32_e64 v4, v3, v4, s[18:19]
	v_fma_f32 v3, -v5, v3, v2
	v_cmp_lt_f32_e64 s[18:19], 0, v3
	s_nop 1
	v_cndmask_b32_e64 v3, v4, v5, s[18:19]
	v_mul_f32_e32 v4, 0x37800000, v3
	v_cndmask_b32_e32 v3, v3, v4, vcc
	v_mov_b32_e32 v4, 0x260
	v_cmp_class_f32_e32 vcc, v2, v4
	s_nop 1
	v_cndmask_b32_e32 v2, v3, v2, vcc
	s_nop 1
	v_add_f32_dpp v3, v2, v2 quad_perm:[1,0,3,2] row_mask:0xf bank_mask:0xf
	s_nop 1
	v_add_f32_dpp v4, v3, v3 quad_perm:[2,3,0,1] row_mask:0xf bank_mask:0xf
	s_nop 1
	v_add_f32_dpp v5, v4, v4 row_half_mirror row_mask:0xf bank_mask:0xf
	s_nop 1
	v_add_f32_dpp v6, v5, v5 row_mirror row_mask:0xf bank_mask:0xf
	s_nop 1
	v_readlane_b32 s12, v6, 0
	v_readlane_b32 s13, v6, 16
	v_readlane_b32 s14, v6, 32
	v_readlane_b32 s15, v6, 48
	s_nop 3
	v_mov_b32_e32 v7, s12
	v_add_f32_e32 v7, s13, v7
	v_mov_b32_e32 v9, s14
	v_add_f32_e32 v9, s15, v9
	v_add_f32_e32 v0, v7, v9
	v_mov_b32_e32 v4, 0
	s_mov_b64 exec, 1
	v_cvt_f64_f32_e32 v[6:7], v0
	v_add_f64 v[8:9], v[6:7], s[4:5]
	global_atomic_add_f64 v[10:11], v4, v[8:9], s[6:7] sc0
	s_waitcnt vmcnt(0)
	v_cmp_le_f64_e32 vcc, s[16:17], v[10:11]
	s_and_saveexec_b64 s[2:3], vcc
	s_cbranch_execz .Lmain_end
	v_add_f64 v[10:11], v[10:11], -s[16:17]
	v_add_f64 v[10:11], v[10:11], v[6:7]
	v_cvt_f32_f64_e32 v0, v[10:11]
	v_mul_f32_e32 v0, 0x38000000, v0
	global_atomic_add_f32 v4, v0, s[10:11]
